# bundle26 + attention: V transposed reads interleaved with the row-max chain (V-read base in v227)
# speedup vs baseline: 1.0029x; 1.0029x over previous
.LBB0_414:
	v_add3_u32 v227, s101, v173, v171
	ds_read_b64_tr_b16 v[90:91], v227 offset:36864
	s_nop 1
	ds_read_b64_tr_b16 v[86:87], v227 offset:36896
	v_max3_f32 v64, v82, s84, v83
	ds_read_b64_tr_b16 v[100:101], v227 offset:36928
	ds_read_b64_tr_b16 v[108:109], v227 offset:36960
	v_max3_f32 v64, v64, v84, v85
	ds_read_b64_tr_b16 v[92:93], v227 offset:39168
	ds_read_b64_tr_b16 v[88:89], v227 offset:39200
	v_max3_f32 v64, v64, v78, v79
	ds_read_b64_tr_b16 v[102:103], v227 offset:39232
	ds_read_b64_tr_b16 v[110:111], v227 offset:39264
	v_max3_f32 v64, v64, v80, v81
	ds_read_b64_tr_b16 v[104:105], v227 offset:41472
	ds_read_b64_tr_b16 v[112:113], v227 offset:41504
	v_max3_f32 v64, v64, v74, v75
	ds_read_b64_tr_b16 v[118:119], v227 offset:41536
	ds_read_b64_tr_b16 v[126:127], v227 offset:41568
	v_max3_f32 v64, v64, v76, v77
	ds_read_b64_tr_b16 v[106:107], v227 offset:43776
	ds_read_b64_tr_b16 v[114:115], v227 offset:43808
	v_max3_f32 v64, v64, v70, v71
	ds_read_b64_tr_b16 v[120:121], v227 offset:43840
	ds_read_b64_tr_b16 v[128:129], v227 offset:43872
	v_max3_f32 v64, v64, v72, v73
	ds_read_b64_tr_b16 v[122:123], v227 offset:46080
	ds_read_b64_tr_b16 v[130:131], v227 offset:46112
	v_max3_f32 v64, v64, v66, v67
	ds_read_b64_tr_b16 v[138:139], v227 offset:46144
	ds_read_b64_tr_b16 v[146:147], v227 offset:46176
	v_max3_f32 v64, v64, v68, v69
	ds_read_b64_tr_b16 v[124:125], v227 offset:48384
	ds_read_b64_tr_b16 v[132:133], v227 offset:48416
	v_max3_f32 v64, v64, v60, v61
	ds_read_b64_tr_b16 v[140:141], v227 offset:48448
	ds_read_b64_tr_b16 v[148:149], v227 offset:48480
	v_max3_f32 v64, v64, v62, v63
	ds_read_b64_tr_b16 v[142:143], v227 offset:50688
	ds_read_b64_tr_b16 v[152:153], v227 offset:50720
	v_max3_f32 v64, v64, v56, v57
	ds_read_b64_tr_b16 v[156:157], v227 offset:50752
	ds_read_b64_tr_b16 v[134:135], v227 offset:50784
	v_max3_f32 v64, v64, v58, v59
	ds_read_b64_tr_b16 v[144:145], v227 offset:52992
	ds_read_b64_tr_b16 v[154:155], v227 offset:53024
	v_max3_f32 v64, v64, v52, v53
	ds_read_b64_tr_b16 v[158:159], v227 offset:53056
	ds_read_b64_tr_b16 v[136:137], v227 offset:53088
	v_max3_f32 v64, v64, v54, v55
	ds_read_b64_tr_b16 v[150:151], v227 offset:55296
	ds_read_b64_tr_b16 v[116:117], v227 offset:55328
	v_max3_f32 v64, v64, v48, v49
	ds_read_b64_tr_b16 v[98:99], v227 offset:55360
	ds_read_b64_tr_b16 v[94:95], v227 offset:55392
	v_max3_f32 v64, v64, v50, v51
	v_mov_b32_e32 v96, v64
	s_nop 1
	v_permlane16_swap_b32_e32 v64, v96
	v_max_f32_e32 v64, v64, v96
	v_mov_b32_e32 v96, v64
	s_nop 1
	v_permlane32_swap_b32_e32 v64, v96
	v_max_f32_e32 v170, v64, v96
	v_pk_add_f32 v[82:83], v[82:83], v[170:171] op_sel_hi:[1,0] neg_lo:[0,1] neg_hi:[0,1]
	v_pk_add_f32 v[84:85], v[84:85], v[170:171] op_sel_hi:[1,0] neg_lo:[0,1] neg_hi:[0,1]
	v_exp_f32_e32 v82, v82
	v_exp_f32_e32 v83, v83
	v_exp_f32_e32 v84, v84
	v_exp_f32_e32 v85, v85
	v_pk_add_f32 v[78:79], v[78:79], v[170:171] op_sel_hi:[1,0] neg_lo:[0,1] neg_hi:[0,1]
	v_pk_add_f32 v[80:81], v[80:81], v[170:171] op_sel_hi:[1,0] neg_lo:[0,1] neg_hi:[0,1]
	v_exp_f32_e32 v78, v78
	v_exp_f32_e32 v79, v79
	v_exp_f32_e32 v80, v80
	v_exp_f32_e32 v81, v81
	v_pk_add_f32 v[74:75], v[74:75], v[170:171] op_sel_hi:[1,0] neg_lo:[0,1] neg_hi:[0,1]
	v_pk_add_f32 v[76:77], v[76:77], v[170:171] op_sel_hi:[1,0] neg_lo:[0,1] neg_hi:[0,1]
	v_exp_f32_e32 v192, v74
	v_exp_f32_e32 v193, v75
	v_pk_add_f32 v[96:97], v[84:85], v[82:83]
	v_exp_f32_e32 v194, v76
	v_exp_f32_e32 v195, v77
	v_pk_add_f32 v[70:71], v[70:71], v[170:171] op_sel_hi:[1,0] neg_lo:[0,1] neg_hi:[0,1]
	v_pk_add_f32 v[74:75], v[78:79], v[96:97]
	v_pk_add_f32 v[72:73], v[72:73], v[170:171] op_sel_hi:[1,0] neg_lo:[0,1] neg_hi:[0,1]
	v_exp_f32_e32 v96, v70
	v_exp_f32_e32 v97, v71
	v_pk_add_f32 v[74:75], v[80:81], v[74:75]
	v_exp_f32_e32 v196, v72
	v_exp_f32_e32 v197, v73
	v_pk_add_f32 v[66:67], v[66:67], v[170:171] op_sel_hi:[1,0] neg_lo:[0,1] neg_hi:[0,1]
	v_pk_add_f32 v[74:75], v[192:193], v[74:75]
	v_pk_add_f32 v[68:69], v[68:69], v[170:171] op_sel_hi:[1,0] neg_lo:[0,1] neg_hi:[0,1]
	v_exp_f32_e32 v198, v66
	v_exp_f32_e32 v199, v67
	v_pk_add_f32 v[74:75], v[194:195], v[74:75]
	v_exp_f32_e32 v200, v68
	v_exp_f32_e32 v201, v69
	v_pk_add_f32 v[66:67], v[96:97], v[74:75]
	v_cvt_pk_bf16_f32 v68, v78, v79
	v_pk_add_f32 v[66:67], v[196:197], v[66:67]
	v_cvt_pk_bf16_f32 v69, v80, v81
	v_pk_add_f32 v[66:67], v[198:199], v[66:67]
	v_pk_add_f32 v[74:75], v[60:61], v[170:171] op_sel_hi:[1,0] neg_lo:[0,1] neg_hi:[0,1]
	v_pk_add_f32 v[202:203], v[200:201], v[66:67]
	v_cvt_pk_bf16_f32 v66, v82, v83
	v_cvt_pk_bf16_f32 v67, v84, v85
	v_pk_add_f32 v[76:77], v[62:63], v[170:171] op_sel_hi:[1,0] neg_lo:[0,1] neg_hi:[0,1]
	v_exp_f32_e32 v78, v74
	s_waitcnt lgkmcnt(14)
	v_mfma_f32_16x16x32_bf16 v[70:73], v[90:93], v[66:69], 0
	v_exp_f32_e32 v79, v75
	v_exp_f32_e32 v80, v76
	v_exp_f32_e32 v81, v77
	v_mfma_f32_16x16x32_bf16 v[60:63], v[86:89], v[66:69], 0
	v_add_f32_e64 v84, v56, -v170
	v_add_f32_e64 v85, v57, -v170
	v_pk_add_f32 v[86:87], v[58:59], v[170:171] op_sel_hi:[1,0] neg_lo:[0,1] neg_hi:[0,1]
	v_exp_f32_e32 v84, v84
	v_mfma_f32_16x16x32_bf16 v[74:77], v[100:103], v[66:69], 0
	v_exp_f32_e32 v85, v85
	v_exp_f32_e32 v86, v86
	v_exp_f32_e32 v87, v87
	v_mfma_f32_16x16x32_bf16 v[56:59], v[108:111], v[66:69], 0
	v_cvt_pk_bf16_f32 v66, v192, v193
	v_cvt_pk_bf16_f32 v67, v194, v195
	v_cvt_pk_bf16_f32 v68, v96, v97
	v_cvt_pk_bf16_f32 v69, v196, v197
	v_pk_add_f32 v[88:89], v[52:53], v[170:171] op_sel_hi:[1,0] neg_lo:[0,1] neg_hi:[0,1]
	v_pk_add_f32 v[82:83], v[78:79], v[202:203]
	v_mfma_f32_16x16x32_bf16 v[70:73], v[104:107], v[66:69], v[70:73]
	v_add_f32_e64 v90, v54, -v170
	v_add_f32_e64 v91, v55, -v170
	v_pk_add_f32 v[82:83], v[80:81], v[82:83]
	v_pk_add_f32 v[48:49], v[48:49], v[170:171] op_sel_hi:[1,0] neg_lo:[0,1] neg_hi:[0,1]
	v_mfma_f32_16x16x32_bf16 v[60:63], v[112:115], v[66:69], v[60:63]
	v_add_f32_e64 v82, v84, v82
	v_add_f32_e64 v83, v85, v83
	s_waitcnt lgkmcnt(1)
	v_mov_b32_e32 v100, v98
	v_pk_add_f32 v[82:83], v[86:87], v[82:83]
	v_mfma_f32_16x16x32_bf16 v[74:77], v[118:121], v[66:69], v[74:77]
	v_mov_b32_e32 v118, v116
	v_mov_b32_e32 v119, v117
	v_mov_b32_e32 v101, v99
	v_mfma_f32_16x16x32_bf16 v[52:55], v[126:129], v[66:69], v[56:59]
	s_waitcnt lgkmcnt(0)
	v_mov_b32_e32 v96, v94
	v_mov_b32_e32 v97, v95
	v_mov_b32_e32 v64, v65
	v_cvt_pk_bf16_f32 v58, v78, v79
	v_exp_f32_e32 v78, v88
	v_exp_f32_e32 v79, v89
	v_cvt_pk_bf16_f32 v56, v198, v199
	v_cvt_pk_bf16_f32 v57, v200, v201
	v_cvt_pk_bf16_f32 v59, v80, v81
	v_exp_f32_e32 v80, v90
	v_exp_f32_e32 v81, v91
	v_mfma_f32_16x16x32_bf16 v[66:69], v[122:125], v[56:59], v[70:73]
	v_add_f32_e64 v82, v78, v82
	v_add_f32_e64 v83, v79, v83
	s_cmp_eq_u32 s30, 1
	s_mov_b32 s23, 0xe800000
	v_mfma_f32_16x16x32_bf16 v[60:63], v[130:133], v[56:59], v[60:63]
	s_cselect_b32 s23, s23, 0x2e800000
	s_cmp_lg_u32 s30, 0
	s_cselect_b32 s23, s23, 0x12800000
	v_mfma_f32_16x16x32_bf16 v[70:73], v[138:141], v[56:59], v[74:77]
	s_add_u32 s36, s42, s23
	s_addc_u32 s37, s43, 0
	s_lshl_b32 s66, s22, 6
	v_pk_add_f32 v[74:75], v[50:51], v[170:171] op_sel_hi:[1,0] neg_lo:[0,1] neg_hi:[0,1]
	v_exp_f32_e32 v76, v48
	v_exp_f32_e32 v77, v49
	v_exp_f32_e32 v74, v74
	v_exp_f32_e32 v75, v75
	v_mfma_f32_16x16x32_bf16 v[48:51], v[146:149], v[56:59], v[52:55]
	s_nop 2
	v_cvt_pk_bf16_f32 v52, v84, v85
	v_cvt_pk_bf16_f32 v53, v86, v87
	v_cvt_pk_bf16_f32 v54, v78, v79
	v_cvt_pk_bf16_f32 v55, v80, v81
	v_pk_add_f32 v[78:79], v[80:81], v[82:83]
	s_nop 0
	v_mfma_f32_16x16x32_bf16 v[56:59], v[142:145], v[52:55], v[66:69]
	v_mfma_f32_16x16x32_bf16 v[66:69], v[152:155], v[52:55], v[60:63]
	v_mov_b32_e32 v152, v150
	v_mov_b32_e32 v153, v151
	s_nop 0
	v_pk_add_f32 v[60:61], v[76:77], v[78:79]
	v_mfma_f32_16x16x32_bf16 v[70:73], v[156:159], v[52:55], v[70:73]
	v_add_f32_e64 v60, v74, v60
	v_add_f32_e64 v61, v75, v61
	v_cvt_pk_bf16_f32 v62, v76, v77
	v_pk_add_f32 v[60:61], v[60:61], v[60:61] op_sel:[0,1] op_sel_hi:[1,0]
	v_mfma_f32_16x16x32_bf16 v[48:51], v[134:137], v[52:55], v[48:51]
	v_mov_b32_e32 v61, v60
	s_nop 1
	v_permlane16_swap_b32_e32 v60, v61
	v_cvt_pk_bf16_f32 v63, v74, v75
	v_add_f32_e32 v74, v60, v61
	s_nop 0
	v_mfma_f32_16x16x32_bf16 v[52:55], v[150:153], v[62:65], v[56:59]
	v_mfma_f32_16x16x32_bf16 v[56:59], v[116:119], v[62:65], v[66:69]
	v_mfma_f32_16x16x32_bf16 v[66:69], v[98:101], v[62:65], v[70:73]
	s_nop 2
	v_mov_b32_e32 v70, v74
	s_nop 1
	v_permlane32_swap_b32_e32 v74, v70
	v_mfma_f32_16x16x32_bf16 v[60:63], v[94:97], v[62:65], v[48:51]
	s_nop 2
	v_add_f32_e32 v48, v74, v70
	v_rcp_f32_e32 v49, v48
	s_nop 0
	v_mul_f32_e32 v206, 0x42800000, v49
	v_add3_u32 v226, s100, v177, v176
	s_waitcnt vmcnt(9)
	ds_write_b128 v226, v[16:19]
	v_pk_mul_f32 v[208:209], v[52:53], v[206:207] op_sel_hi:[1,0]
	v_pk_mul_f32 v[210:211], v[54:55], v[206:207] op_sel_hi:[1,0]
	v_pk_mul_f32 v[212:213], v[56:57], v[206:207] op_sel_hi:[1,0]
	v_pk_mul_f32 v[216:217], v[58:59], v[206:207] op_sel_hi:[1,0]
	s_waitcnt vmcnt(8)
	ds_write_b128 v226, v[20:23] offset:36864
	v_pk_mul_f32 v[218:219], v[66:67], v[206:207] op_sel_hi:[1,0]
	v_pk_mul_f32 v[220:221], v[68:69], v[206:207] op_sel_hi:[1,0]
	v_pk_mul_f32 v[222:223], v[60:61], v[206:207] op_sel_hi:[1,0]
	v_pk_mul_f32 v[224:225], v[62:63], v[206:207] op_sel_hi:[1,0]
	v_add3_u32 v226, s100, v178, v176
	s_waitcnt vmcnt(7)
	ds_write_b128 v226, v[24:27]
	v_med3_f32 v208, v208, s55, v228
	v_med3_f32 v209, v209, s55, v228
	v_med3_f32 v210, v210, s55, v228
	v_med3_f32 v211, v211, s55, v228
	s_waitcnt vmcnt(6)
	ds_write_b128 v226, v[28:31] offset:36864
	v_med3_f32 v212, v212, s55, v228
	v_med3_f32 v213, v213, s55, v228
	v_med3_f32 v216, v216, s55, v228
	v_med3_f32 v217, v217, s55, v228
	v_add3_u32 v226, s100, v179, v176
	s_waitcnt vmcnt(5)
	ds_write_b128 v226, v[32:35]
	v_med3_f32 v218, v218, s55, v228
	v_med3_f32 v219, v219, s55, v228
	v_med3_f32 v220, v220, s55, v228
	v_med3_f32 v221, v221, s55, v228
	s_waitcnt vmcnt(4)
	ds_write_b128 v226, v[36:39] offset:36864
	v_med3_f32 v222, v222, s55, v228
	v_med3_f32 v223, v223, s55, v228
	v_med3_f32 v224, v224, s55, v228
	v_med3_f32 v225, v225, s55, v228
	v_add3_u32 v226, s100, v180, v176
	s_waitcnt vmcnt(3)
	ds_write_b128 v226, v[40:43]
	v_cvt_pk_fp8_f32 v50, v208, v209
	v_cvt_pk_fp8_f32 v50, v210, v211 op_sel:[0,0,1]
	v_cvt_pk_fp8_f32 v51, v212, v213
	v_cvt_pk_fp8_f32 v51, v216, v217 op_sel:[0,0,1]
	s_waitcnt vmcnt(2)
	ds_write_b128 v226, v[44:47] offset:36864
	v_cvt_pk_fp8_f32 v52, v218, v219
	v_cvt_pk_fp8_f32 v52, v220, v221 op_sel:[0,0,1]
	v_cvt_pk_fp8_f32 v53, v222, v223
	v_cvt_pk_fp8_f32 v53, v224, v225 op_sel:[0,0,1]
	v_lshlrev_b64 v[54:55], 10, v[166:167]
	v_lshl_add_u64 v[54:55], s[36:37], 0, v[54:55]
	v_lshl_add_u64 v[54:55], v[54:55], 0, s[66:67]
	v_lshl_add_u64 v[54:55], v[54:55], 0, v[160:161]
	global_store_dwordx4 v[54:55], v[50:53], off sc1
	s_and_saveexec_b64 s[36:37], vcc
	s_cbranch_execz .LBB0_416
	v_log_f32_e32 v48, v48
	s_ashr_i32 s31, s30, 31
	s_lshl_b64 s[30:31], s[30:31], 22
	v_readlane_b32 s23, v254, 30
	s_add_u32 s30, s23, s30
	v_readlane_b32 s23, v254, 31
	v_add_f32_e32 v48, v170, v48
	s_addc_u32 s31, s23, s31
	v_mul_f32_e32 v50, 0x3f317218, v48
	v_lshlrev_b64 v[48:49], 6, v[166:167]
	v_lshl_add_u64 v[48:49], s[30:31], 0, v[48:49]
	s_mov_b32 s23, s67
	v_lshl_add_u64 v[48:49], s[22:23], 2, v[48:49]
	global_store_dword v[48:49], v50, off
